# speedup vs baseline: 1.0225x; 1.0225x over previous
.LBB1_11:
	v_exp_f32_e32 v3, v18
	v_exp_f32_e32 v4, v19
	v_exp_f32_e32 v5, v20
	v_exp_f32_e32 v6, v21
	v_exp_f32_e32 v7, v22
	v_exp_f32_e32 v8, v23
	v_exp_f32_e32 v9, v24
	v_exp_f32_e32 v10, v25
	s_waitcnt vmcnt(20)
	v_cmp_lt_f32_e64 s[38:39], s37, v203
	v_cmp_lt_f32_e64 s[42:43], s37, v205
	v_cmp_lt_f32_e64 s[48:49], s37, v207
	v_cmp_lt_f32_e64 s[50:51], s37, v210
	v_addc_co_u32_e64 v2, s[54:55], v2, v2, s[38:39]
	v_cndmask_b32_e64 v3, v3, 0, s[38:39]
	v_addc_co_u32_e64 v2, s[54:55], v2, v2, s[42:43]
	v_cndmask_b32_e64 v4, v4, 0, s[42:43]
	v_addc_co_u32_e64 v2, s[54:55], v2, v2, s[48:49]
	v_cndmask_b32_e64 v5, v5, 0, s[48:49]
	v_addc_co_u32_e64 v2, s[54:55], v2, v2, s[50:51]
	v_cndmask_b32_e64 v6, v6, 0, s[50:51]
	v_add_f32 v179, v179, v3
	v_add_f32 v178, v178, v4
	v_add_f32 v177, v177, v5
	v_add_f32 v176, v176, v6

	s_lshl_b32 s34, s36, 8
	v_readlane_b32 s36, v240, 14
	v_exp_f32_e32 v11, v26
	v_exp_f32_e32 v12, v27
	v_exp_f32_e32 v13, v28
	v_exp_f32_e32 v14, v29
	s_waitcnt vmcnt(16)
	v_cmp_lt_f32_e64 s[38:39], s37, v204
	v_cmp_lt_f32_e64 s[42:43], s37, v206
	v_cmp_lt_f32_e64 s[48:49], s37, v208
	v_cmp_lt_f32_e64 s[50:51], s37, v211
	v_addc_co_u32_e64 v2, s[54:55], v2, v2, s[38:39]
	v_cndmask_b32_e64 v7, v7, 0, s[38:39]
	v_addc_co_u32_e64 v2, s[54:55], v2, v2, s[42:43]
	v_cndmask_b32_e64 v8, v8, 0, s[42:43]
	v_addc_co_u32_e64 v2, s[54:55], v2, v2, s[48:49]
	v_cndmask_b32_e64 v9, v9, 0, s[48:49]
	v_addc_co_u32_e64 v2, s[54:55], v2, v2, s[50:51]
	v_cndmask_b32_e64 v10, v10, 0, s[50:51]
	v_add_f32 v175, v175, v7
	v_add_f32 v174, v174, v8
	v_add_f32 v173, v173, v9
	v_add_f32 v172, v172, v10

	s_add_i32 s34, s36, s34
	v_exp_f32_e32 v15, v30
	v_exp_f32_e32 v16, v31
	v_exp_f32_e32 v17, v32
	v_exp_f32_e32 v18, v33
	s_waitcnt vmcnt(12)
	v_cmp_lt_f32_e64 s[38:39], s37, v212
	v_cmp_lt_f32_e64 s[42:43], s37, v213
	v_cmp_lt_f32_e64 s[48:49], s37, v214
	v_cmp_lt_f32_e64 s[50:51], s37, v215
	v_addc_co_u32_e64 v2, s[54:55], v2, v2, s[38:39]
	v_cndmask_b32_e64 v11, v11, 0, s[38:39]
	v_addc_co_u32_e64 v2, s[54:55], v2, v2, s[42:43]
	v_cndmask_b32_e64 v12, v12, 0, s[42:43]
	v_addc_co_u32_e64 v2, s[54:55], v2, v2, s[48:49]
	v_cndmask_b32_e64 v13, v13, 0, s[48:49]
	v_addc_co_u32_e64 v2, s[54:55], v2, v2, s[50:51]
	v_cndmask_b32_e64 v14, v14, 0, s[50:51]
	v_add_f32 v171, v171, v11
	v_add_f32 v170, v170, v12
	v_add_f32 v169, v169, v13
	v_add_f32 v168, v168, v14

	v_lshl_add_u32 v3, v194, 2, s34
	s_waitcnt vmcnt(8)
	v_cmp_lt_f32_e64 s[38:39], s37, v190
	v_cmp_lt_f32_e64 s[42:43], s37, v192
	v_cmp_lt_f32_e64 s[48:49], s37, v193
	v_cmp_lt_f32_e64 s[50:51], s37, v202
	v_addc_co_u32_e64 v2, s[54:55], v2, v2, s[38:39]
	v_cndmask_b32_e64 v15, v15, 0, s[38:39]
	v_addc_co_u32_e64 v2, s[54:55], v2, v2, s[42:43]
	v_cndmask_b32_e64 v16, v16, 0, s[42:43]
	v_addc_co_u32_e64 v2, s[54:55], v2, v2, s[48:49]
	v_cndmask_b32_e64 v17, v17, 0, s[48:49]
	v_addc_co_u32_e64 v2, s[54:55], v2, v2, s[50:51]
	v_cndmask_b32_e64 v18, v18, 0, s[50:51]
	v_add_f32 v167, v167, v15
	v_add_f32 v166, v166, v16
	v_add_f32 v165, v165, v17
	v_add_f32 v164, v164, v18

	ds_write_b32 v3, v2
	s_lshl_b32 s38, s52, 8
	s_add_i32 s34, s38, 0x8800
	s_add_i32 s38, s38, 0x8000
	v_cmp_eq_u32_e32 vcc, 16, v163
	v_lshl_add_u32 v3, v160, 2, s34
	v_lshl_add_u32 v152, v160, 2, s38
	v_add_f32_dpp v227, v227, v227 quad_perm:[1,0,3,2] row_mask:0xf bank_mask:0xf bound_ctrl:1
	v_add_f32_dpp v224, v224, v224 quad_perm:[1,0,3,2] row_mask:0xf bank_mask:0xf bound_ctrl:1
	v_add_f32_dpp v217, v217, v217 quad_perm:[1,0,3,2] row_mask:0xf bank_mask:0xf bound_ctrl:1
	v_add_f32_dpp v216, v216, v216 quad_perm:[1,0,3,2] row_mask:0xf bank_mask:0xf bound_ctrl:1
	v_add_f32_dpp v209, v209, v209 quad_perm:[1,0,3,2] row_mask:0xf bank_mask:0xf bound_ctrl:1
	v_add_f32_dpp v191, v191, v191 quad_perm:[1,0,3,2] row_mask:0xf bank_mask:0xf bound_ctrl:1
	v_add_f32_dpp v189, v189, v189 quad_perm:[1,0,3,2] row_mask:0xf bank_mask:0xf bound_ctrl:1
	v_add_f32_dpp v188, v188, v188 quad_perm:[1,0,3,2] row_mask:0xf bank_mask:0xf bound_ctrl:1
	v_add_f32_dpp v187, v187, v187 quad_perm:[1,0,3,2] row_mask:0xf bank_mask:0xf bound_ctrl:1
	v_add_f32_dpp v186, v186, v186 quad_perm:[1,0,3,2] row_mask:0xf bank_mask:0xf bound_ctrl:1
	v_add_f32_dpp v185, v185, v185 quad_perm:[1,0,3,2] row_mask:0xf bank_mask:0xf bound_ctrl:1
	v_add_f32_dpp v184, v184, v184 quad_perm:[1,0,3,2] row_mask:0xf bank_mask:0xf bound_ctrl:1
	v_add_f32_dpp v183, v183, v183 quad_perm:[1,0,3,2] row_mask:0xf bank_mask:0xf bound_ctrl:1
	v_add_f32_dpp v182, v182, v182 quad_perm:[1,0,3,2] row_mask:0xf bank_mask:0xf bound_ctrl:1
	v_add_f32_dpp v181, v181, v181 quad_perm:[1,0,3,2] row_mask:0xf bank_mask:0xf bound_ctrl:1
	v_add_f32_dpp v180, v180, v180 quad_perm:[1,0,3,2] row_mask:0xf bank_mask:0xf bound_ctrl:1
	v_add_f32_dpp v179, v179, v179 quad_perm:[1,0,3,2] row_mask:0xf bank_mask:0xf bound_ctrl:1
	v_add_f32_dpp v178, v178, v178 quad_perm:[1,0,3,2] row_mask:0xf bank_mask:0xf bound_ctrl:1
	v_add_f32_dpp v177, v177, v177 quad_perm:[1,0,3,2] row_mask:0xf bank_mask:0xf bound_ctrl:1
	v_add_f32_dpp v176, v176, v176 quad_perm:[1,0,3,2] row_mask:0xf bank_mask:0xf bound_ctrl:1
	v_add_f32_dpp v175, v175, v175 quad_perm:[1,0,3,2] row_mask:0xf bank_mask:0xf bound_ctrl:1
	v_add_f32_dpp v174, v174, v174 quad_perm:[1,0,3,2] row_mask:0xf bank_mask:0xf bound_ctrl:1
	v_add_f32_dpp v173, v173, v173 quad_perm:[1,0,3,2] row_mask:0xf bank_mask:0xf bound_ctrl:1
	v_add_f32_dpp v172, v172, v172 quad_perm:[1,0,3,2] row_mask:0xf bank_mask:0xf bound_ctrl:1
	v_add_f32_dpp v171, v171, v171 quad_perm:[1,0,3,2] row_mask:0xf bank_mask:0xf bound_ctrl:1
	v_add_f32_dpp v170, v170, v170 quad_perm:[1,0,3,2] row_mask:0xf bank_mask:0xf bound_ctrl:1
	v_add_f32_dpp v169, v169, v169 quad_perm:[1,0,3,2] row_mask:0xf bank_mask:0xf bound_ctrl:1
	v_add_f32_dpp v168, v168, v168 quad_perm:[1,0,3,2] row_mask:0xf bank_mask:0xf bound_ctrl:1
	v_add_f32_dpp v167, v167, v167 quad_perm:[1,0,3,2] row_mask:0xf bank_mask:0xf bound_ctrl:1
	v_add_f32_dpp v166, v166, v166 quad_perm:[1,0,3,2] row_mask:0xf bank_mask:0xf bound_ctrl:1
	v_add_f32_dpp v165, v165, v165 quad_perm:[1,0,3,2] row_mask:0xf bank_mask:0xf bound_ctrl:1
	v_add_f32_dpp v164, v164, v164 quad_perm:[1,0,3,2] row_mask:0xf bank_mask:0xf bound_ctrl:1
	v_add_f32_dpp v227, v227, v227 quad_perm:[2,3,0,1] row_mask:0xf bank_mask:0xf bound_ctrl:1
	v_add_f32_dpp v224, v224, v224 quad_perm:[2,3,0,1] row_mask:0xf bank_mask:0xf bound_ctrl:1
	v_add_f32_dpp v217, v217, v217 quad_perm:[2,3,0,1] row_mask:0xf bank_mask:0xf bound_ctrl:1
	v_add_f32_dpp v216, v216, v216 quad_perm:[2,3,0,1] row_mask:0xf bank_mask:0xf bound_ctrl:1
	v_add_f32_dpp v209, v209, v209 quad_perm:[2,3,0,1] row_mask:0xf bank_mask:0xf bound_ctrl:1
	v_add_f32_dpp v191, v191, v191 quad_perm:[2,3,0,1] row_mask:0xf bank_mask:0xf bound_ctrl:1
	v_add_f32_dpp v189, v189, v189 quad_perm:[2,3,0,1] row_mask:0xf bank_mask:0xf bound_ctrl:1
	v_add_f32_dpp v188, v188, v188 quad_perm:[2,3,0,1] row_mask:0xf bank_mask:0xf bound_ctrl:1
	v_add_f32_dpp v187, v187, v187 quad_perm:[2,3,0,1] row_mask:0xf bank_mask:0xf bound_ctrl:1
	v_add_f32_dpp v186, v186, v186 quad_perm:[2,3,0,1] row_mask:0xf bank_mask:0xf bound_ctrl:1
	v_add_f32_dpp v185, v185, v185 quad_perm:[2,3,0,1] row_mask:0xf bank_mask:0xf bound_ctrl:1
	v_add_f32_dpp v184, v184, v184 quad_perm:[2,3,0,1] row_mask:0xf bank_mask:0xf bound_ctrl:1
	v_add_f32_dpp v183, v183, v183 quad_perm:[2,3,0,1] row_mask:0xf bank_mask:0xf bound_ctrl:1
	v_add_f32_dpp v182, v182, v182 quad_perm:[2,3,0,1] row_mask:0xf bank_mask:0xf bound_ctrl:1
	v_add_f32_dpp v181, v181, v181 quad_perm:[2,3,0,1] row_mask:0xf bank_mask:0xf bound_ctrl:1
	v_add_f32_dpp v180, v180, v180 quad_perm:[2,3,0,1] row_mask:0xf bank_mask:0xf bound_ctrl:1
	v_add_f32_dpp v179, v179, v179 quad_perm:[2,3,0,1] row_mask:0xf bank_mask:0xf bound_ctrl:1
	v_add_f32_dpp v178, v178, v178 quad_perm:[2,3,0,1] row_mask:0xf bank_mask:0xf bound_ctrl:1
	v_add_f32_dpp v177, v177, v177 quad_perm:[2,3,0,1] row_mask:0xf bank_mask:0xf bound_ctrl:1
	v_add_f32_dpp v176, v176, v176 quad_perm:[2,3,0,1] row_mask:0xf bank_mask:0xf bound_ctrl:1
	v_add_f32_dpp v175, v175, v175 quad_perm:[2,3,0,1] row_mask:0xf bank_mask:0xf bound_ctrl:1
	v_add_f32_dpp v174, v174, v174 quad_perm:[2,3,0,1] row_mask:0xf bank_mask:0xf bound_ctrl:1
	v_add_f32_dpp v173, v173, v173 quad_perm:[2,3,0,1] row_mask:0xf bank_mask:0xf bound_ctrl:1
	v_add_f32_dpp v172, v172, v172 quad_perm:[2,3,0,1] row_mask:0xf bank_mask:0xf bound_ctrl:1
	v_add_f32_dpp v171, v171, v171 quad_perm:[2,3,0,1] row_mask:0xf bank_mask:0xf bound_ctrl:1
	v_add_f32_dpp v170, v170, v170 quad_perm:[2,3,0,1] row_mask:0xf bank_mask:0xf bound_ctrl:1
	v_add_f32_dpp v169, v169, v169 quad_perm:[2,3,0,1] row_mask:0xf bank_mask:0xf bound_ctrl:1
	v_add_f32_dpp v168, v168, v168 quad_perm:[2,3,0,1] row_mask:0xf bank_mask:0xf bound_ctrl:1
	v_add_f32_dpp v167, v167, v167 quad_perm:[2,3,0,1] row_mask:0xf bank_mask:0xf bound_ctrl:1
	v_add_f32_dpp v166, v166, v166 quad_perm:[2,3,0,1] row_mask:0xf bank_mask:0xf bound_ctrl:1
	v_add_f32_dpp v165, v165, v165 quad_perm:[2,3,0,1] row_mask:0xf bank_mask:0xf bound_ctrl:1
	v_add_f32_dpp v164, v164, v164 quad_perm:[2,3,0,1] row_mask:0xf bank_mask:0xf bound_ctrl:1
	v_add_f32_dpp v227, v227, v227 row_half_mirror row_mask:0xf bank_mask:0xf bound_ctrl:1
	v_add_f32_dpp v224, v224, v224 row_half_mirror row_mask:0xf bank_mask:0xf bound_ctrl:1
	v_add_f32_dpp v217, v217, v217 row_half_mirror row_mask:0xf bank_mask:0xf bound_ctrl:1
	v_add_f32_dpp v216, v216, v216 row_half_mirror row_mask:0xf bank_mask:0xf bound_ctrl:1
	v_add_f32_dpp v209, v209, v209 row_half_mirror row_mask:0xf bank_mask:0xf bound_ctrl:1
	v_add_f32_dpp v191, v191, v191 row_half_mirror row_mask:0xf bank_mask:0xf bound_ctrl:1
	v_add_f32_dpp v189, v189, v189 row_half_mirror row_mask:0xf bank_mask:0xf bound_ctrl:1
	v_add_f32_dpp v188, v188, v188 row_half_mirror row_mask:0xf bank_mask:0xf bound_ctrl:1
	v_add_f32_dpp v187, v187, v187 row_half_mirror row_mask:0xf bank_mask:0xf bound_ctrl:1
	v_add_f32_dpp v186, v186, v186 row_half_mirror row_mask:0xf bank_mask:0xf bound_ctrl:1
	v_add_f32_dpp v185, v185, v185 row_half_mirror row_mask:0xf bank_mask:0xf bound_ctrl:1
	v_add_f32_dpp v184, v184, v184 row_half_mirror row_mask:0xf bank_mask:0xf bound_ctrl:1
	v_add_f32_dpp v183, v183, v183 row_half_mirror row_mask:0xf bank_mask:0xf bound_ctrl:1
	v_add_f32_dpp v182, v182, v182 row_half_mirror row_mask:0xf bank_mask:0xf bound_ctrl:1
	v_add_f32_dpp v181, v181, v181 row_half_mirror row_mask:0xf bank_mask:0xf bound_ctrl:1
	v_add_f32_dpp v180, v180, v180 row_half_mirror row_mask:0xf bank_mask:0xf bound_ctrl:1
	v_add_f32_dpp v179, v179, v179 row_half_mirror row_mask:0xf bank_mask:0xf bound_ctrl:1
	v_add_f32_dpp v178, v178, v178 row_half_mirror row_mask:0xf bank_mask:0xf bound_ctrl:1
	v_add_f32_dpp v177, v177, v177 row_half_mirror row_mask:0xf bank_mask:0xf bound_ctrl:1
	v_add_f32_dpp v176, v176, v176 row_half_mirror row_mask:0xf bank_mask:0xf bound_ctrl:1
	v_add_f32_dpp v175, v175, v175 row_half_mirror row_mask:0xf bank_mask:0xf bound_ctrl:1
	v_add_f32_dpp v174, v174, v174 row_half_mirror row_mask:0xf bank_mask:0xf bound_ctrl:1
	v_add_f32_dpp v173, v173, v173 row_half_mirror row_mask:0xf bank_mask:0xf bound_ctrl:1
	v_add_f32_dpp v172, v172, v172 row_half_mirror row_mask:0xf bank_mask:0xf bound_ctrl:1
	v_add_f32_dpp v171, v171, v171 row_half_mirror row_mask:0xf bank_mask:0xf bound_ctrl:1
	v_add_f32_dpp v170, v170, v170 row_half_mirror row_mask:0xf bank_mask:0xf bound_ctrl:1
	v_add_f32_dpp v169, v169, v169 row_half_mirror row_mask:0xf bank_mask:0xf bound_ctrl:1
	v_add_f32_dpp v168, v168, v168 row_half_mirror row_mask:0xf bank_mask:0xf bound_ctrl:1
	v_add_f32_dpp v167, v167, v167 row_half_mirror row_mask:0xf bank_mask:0xf bound_ctrl:1
	v_add_f32_dpp v166, v166, v166 row_half_mirror row_mask:0xf bank_mask:0xf bound_ctrl:1
	v_add_f32_dpp v165, v165, v165 row_half_mirror row_mask:0xf bank_mask:0xf bound_ctrl:1
	v_add_f32_dpp v164, v164, v164 row_half_mirror row_mask:0xf bank_mask:0xf bound_ctrl:1
	v_add_f32_dpp v227, v227, v227 row_mirror row_mask:0xf bank_mask:0xf bound_ctrl:1
	v_add_f32_dpp v224, v224, v224 row_mirror row_mask:0xf bank_mask:0xf bound_ctrl:1
	v_add_f32_dpp v217, v217, v217 row_mirror row_mask:0xf bank_mask:0xf bound_ctrl:1
	v_add_f32_dpp v216, v216, v216 row_mirror row_mask:0xf bank_mask:0xf bound_ctrl:1
	v_add_f32_dpp v209, v209, v209 row_mirror row_mask:0xf bank_mask:0xf bound_ctrl:1
	v_add_f32_dpp v191, v191, v191 row_mirror row_mask:0xf bank_mask:0xf bound_ctrl:1
	v_add_f32_dpp v189, v189, v189 row_mirror row_mask:0xf bank_mask:0xf bound_ctrl:1
	v_add_f32_dpp v188, v188, v188 row_mirror row_mask:0xf bank_mask:0xf bound_ctrl:1
	v_add_f32_dpp v187, v187, v187 row_mirror row_mask:0xf bank_mask:0xf bound_ctrl:1
	v_add_f32_dpp v186, v186, v186 row_mirror row_mask:0xf bank_mask:0xf bound_ctrl:1
	v_add_f32_dpp v185, v185, v185 row_mirror row_mask:0xf bank_mask:0xf bound_ctrl:1
	v_add_f32_dpp v184, v184, v184 row_mirror row_mask:0xf bank_mask:0xf bound_ctrl:1
	v_add_f32_dpp v183, v183, v183 row_mirror row_mask:0xf bank_mask:0xf bound_ctrl:1
	v_add_f32_dpp v182, v182, v182 row_mirror row_mask:0xf bank_mask:0xf bound_ctrl:1
	v_add_f32_dpp v181, v181, v181 row_mirror row_mask:0xf bank_mask:0xf bound_ctrl:1
	v_add_f32_dpp v180, v180, v180 row_mirror row_mask:0xf bank_mask:0xf bound_ctrl:1
	v_add_f32_dpp v179, v179, v179 row_mirror row_mask:0xf bank_mask:0xf bound_ctrl:1
	v_add_f32_dpp v178, v178, v178 row_mirror row_mask:0xf bank_mask:0xf bound_ctrl:1
	v_add_f32_dpp v177, v177, v177 row_mirror row_mask:0xf bank_mask:0xf bound_ctrl:1
	v_add_f32_dpp v176, v176, v176 row_mirror row_mask:0xf bank_mask:0xf bound_ctrl:1
	v_add_f32_dpp v175, v175, v175 row_mirror row_mask:0xf bank_mask:0xf bound_ctrl:1
	v_add_f32_dpp v174, v174, v174 row_mirror row_mask:0xf bank_mask:0xf bound_ctrl:1
	v_add_f32_dpp v173, v173, v173 row_mirror row_mask:0xf bank_mask:0xf bound_ctrl:1
	v_add_f32_dpp v172, v172, v172 row_mirror row_mask:0xf bank_mask:0xf bound_ctrl:1
	v_add_f32_dpp v171, v171, v171 row_mirror row_mask:0xf bank_mask:0xf bound_ctrl:1
	v_add_f32_dpp v170, v170, v170 row_mirror row_mask:0xf bank_mask:0xf bound_ctrl:1
	v_add_f32_dpp v169, v169, v169 row_mirror row_mask:0xf bank_mask:0xf bound_ctrl:1
	v_add_f32_dpp v168, v168, v168 row_mirror row_mask:0xf bank_mask:0xf bound_ctrl:1
	v_add_f32_dpp v167, v167, v167 row_mirror row_mask:0xf bank_mask:0xf bound_ctrl:1
	v_add_f32_dpp v166, v166, v166 row_mirror row_mask:0xf bank_mask:0xf bound_ctrl:1
	v_add_f32_dpp v165, v165, v165 row_mirror row_mask:0xf bank_mask:0xf bound_ctrl:1
	v_add_f32_dpp v164, v164, v164 row_mirror row_mask:0xf bank_mask:0xf bound_ctrl:1
	v_mov_b32_dpp v4, v227 row_bcast:15 row_mask:0xa bank_mask:0xf bound_ctrl:1
	v_mov_b32_dpp v5, v224 row_bcast:15 row_mask:0xa bank_mask:0xf bound_ctrl:1
	v_mov_b32_dpp v6, v217 row_bcast:15 row_mask:0xa bank_mask:0xf bound_ctrl:1
	v_mov_b32_dpp v7, v216 row_bcast:15 row_mask:0xa bank_mask:0xf bound_ctrl:1
	v_mov_b32_dpp v8, v209 row_bcast:15 row_mask:0xa bank_mask:0xf bound_ctrl:1
	v_mov_b32_dpp v9, v191 row_bcast:15 row_mask:0xa bank_mask:0xf bound_ctrl:1
	v_mov_b32_dpp v10, v189 row_bcast:15 row_mask:0xa bank_mask:0xf bound_ctrl:1
	v_mov_b32_dpp v11, v188 row_bcast:15 row_mask:0xa bank_mask:0xf bound_ctrl:1
	v_mov_b32_dpp v12, v187 row_bcast:15 row_mask:0xa bank_mask:0xf bound_ctrl:1
	v_mov_b32_dpp v13, v186 row_bcast:15 row_mask:0xa bank_mask:0xf bound_ctrl:1
	v_mov_b32_dpp v14, v185 row_bcast:15 row_mask:0xa bank_mask:0xf bound_ctrl:1
	v_mov_b32_dpp v15, v184 row_bcast:15 row_mask:0xa bank_mask:0xf bound_ctrl:1
	v_mov_b32_dpp v16, v183 row_bcast:15 row_mask:0xa bank_mask:0xf bound_ctrl:1
	v_mov_b32_dpp v17, v182 row_bcast:15 row_mask:0xa bank_mask:0xf bound_ctrl:1
	v_mov_b32_dpp v18, v181 row_bcast:15 row_mask:0xa bank_mask:0xf bound_ctrl:1
	v_mov_b32_dpp v19, v180 row_bcast:15 row_mask:0xa bank_mask:0xf bound_ctrl:1
	v_mov_b32_dpp v20, v179 row_bcast:15 row_mask:0xa bank_mask:0xf bound_ctrl:1
	v_mov_b32_dpp v21, v178 row_bcast:15 row_mask:0xa bank_mask:0xf bound_ctrl:1
	v_mov_b32_dpp v22, v177 row_bcast:15 row_mask:0xa bank_mask:0xf bound_ctrl:1
	v_mov_b32_dpp v23, v176 row_bcast:15 row_mask:0xa bank_mask:0xf bound_ctrl:1
	v_mov_b32_dpp v24, v175 row_bcast:15 row_mask:0xa bank_mask:0xf bound_ctrl:1
	v_mov_b32_dpp v25, v174 row_bcast:15 row_mask:0xa bank_mask:0xf bound_ctrl:1
	v_mov_b32_dpp v26, v173 row_bcast:15 row_mask:0xa bank_mask:0xf bound_ctrl:1
	v_mov_b32_dpp v27, v172 row_bcast:15 row_mask:0xa bank_mask:0xf bound_ctrl:1
	v_mov_b32_dpp v28, v171 row_bcast:15 row_mask:0xa bank_mask:0xf bound_ctrl:1
	v_mov_b32_dpp v29, v170 row_bcast:15 row_mask:0xa bank_mask:0xf bound_ctrl:1
	v_mov_b32_dpp v30, v169 row_bcast:15 row_mask:0xa bank_mask:0xf bound_ctrl:1
	v_mov_b32_dpp v31, v168 row_bcast:15 row_mask:0xa bank_mask:0xf bound_ctrl:1
	v_mov_b32_dpp v32, v167 row_bcast:15 row_mask:0xa bank_mask:0xf bound_ctrl:1
	v_mov_b32_dpp v33, v166 row_bcast:15 row_mask:0xa bank_mask:0xf bound_ctrl:1
	v_mov_b32_dpp v130, v165 row_bcast:15 row_mask:0xa bank_mask:0xf bound_ctrl:1
	v_mov_b32_dpp v131, v164 row_bcast:15 row_mask:0xa bank_mask:0xf bound_ctrl:1
	s_and_saveexec_b64 s[36:37], vcc
	v_add_f32_e32 v227, v227, v4
	v_add_f32_e32 v224, v224, v5
	v_add_f32_e32 v217, v217, v6
	v_add_f32_e32 v216, v216, v7
	v_add_f32_e32 v209, v209, v8
	v_add_f32_e32 v191, v191, v9
	v_add_f32_e32 v189, v189, v10
	v_add_f32_e32 v188, v188, v11
	v_add_f32_e32 v187, v187, v12
	v_add_f32_e32 v186, v186, v13
	v_add_f32_e32 v185, v185, v14
	v_add_f32_e32 v184, v184, v15
	v_add_f32_e32 v183, v183, v16
	v_add_f32_e32 v182, v182, v17
	v_add_f32_e32 v181, v181, v18
	v_add_f32_e32 v180, v180, v19
	v_add_f32_e32 v179, v179, v20
	v_add_f32_e32 v178, v178, v21
	v_add_f32_e32 v177, v177, v22
	v_add_f32_e32 v176, v176, v23
	v_add_f32_e32 v175, v175, v24
	v_add_f32_e32 v174, v174, v25
	v_add_f32_e32 v173, v173, v26
	v_add_f32_e32 v172, v172, v27
	v_add_f32_e32 v171, v171, v28
	v_add_f32_e32 v170, v170, v29
	v_add_f32_e32 v169, v169, v30
	v_add_f32_e32 v168, v168, v31
	v_add_f32_e32 v167, v167, v32
	v_add_f32_e32 v166, v166, v33
	v_add_f32_e32 v165, v165, v130
	v_add_f32_e32 v164, v164, v131
	ds_write_b32 v3, v227
	ds_write_b32 v3, v224 offset:4
	ds_write_b32 v3, v217 offset:8
	ds_write_b32 v3, v216 offset:12
	ds_write_b32 v3, v209 offset:32
	ds_write_b32 v3, v191 offset:36
	ds_write_b32 v3, v189 offset:40
	ds_write_b32 v3, v188 offset:44
	ds_write_b32 v3, v187 offset:64
	ds_write_b32 v3, v186 offset:68
	ds_write_b32 v3, v185 offset:72
	ds_write_b32 v3, v184 offset:76
	ds_write_b32 v3, v183 offset:96
	ds_write_b32 v3, v182 offset:100
	ds_write_b32 v3, v181 offset:104
	ds_write_b32 v3, v180 offset:108
	ds_write_b32 v3, v179 offset:128
	ds_write_b32 v3, v178 offset:132
	ds_write_b32 v3, v177 offset:136
	ds_write_b32 v3, v176 offset:140
	ds_write_b32 v3, v175 offset:160
	ds_write_b32 v3, v174 offset:164
	ds_write_b32 v3, v173 offset:168
	ds_write_b32 v3, v172 offset:172
	ds_write_b32 v3, v171 offset:192
	ds_write_b32 v3, v170 offset:196
	ds_write_b32 v3, v169 offset:200
	ds_write_b32 v3, v168 offset:204
	ds_write_b32 v3, v167 offset:224
	ds_write_b32 v3, v166 offset:228
	ds_write_b32 v3, v165 offset:232
	ds_write_b32 v3, v164 offset:236
	s_or_b64 exec, exec, s[36:37]
	v_lshrrev_b32_e32 v4, 4, v2
	v_and_b32_e32 v5, 0x1010101, v2
	v_and_b32_e32 v6, 0x1010101, v4
	v_add_u32_e32 v162, v162, v5
	v_add_u32_e32 v157, v157, v6
	v_and_b32_e32 v5, 0x2020202, v2
	v_and_b32_e32 v6, 0x2020202, v4
	v_add_u32_e32 v161, v161, v5
	v_add_u32_e32 v156, v156, v6
	v_and_b32_e32 v5, 0x4040404, v2
	v_and_b32_e32 v6, 0x4040404, v4
	v_add_u32_e32 v159, v159, v5
	v_add_u32_e32 v155, v155, v6
	v_and_b32_e32 v5, 0x8080808, v2
	v_and_b32_e32 v6, 0x8080808, v4
	v_add_u32_e32 v158, v158, v5
	v_add_u32_e32 v154, v154, v6
	v_lshrrev_b32_e32 v161, 1, v161
	v_lshrrev_b32_e32 v159, 2, v159
	v_lshrrev_b32_e32 v158, 3, v158
	v_lshrrev_b32_e32 v156, 1, v156
	v_lshrrev_b32_e32 v155, 2, v155
	v_lshrrev_b32_e32 v154, 3, v154
	v_and_b32_e32 v8, 0xff00ff, v162
	v_lshrrev_b32_e32 v16, 8, v162
	v_and_b32_e32 v9, 0xff00ff, v161
	v_lshrrev_b32_e32 v17, 8, v161
	v_and_b32_e32 v10, 0xff00ff, v159
	v_lshrrev_b32_e32 v18, 8, v159
	v_and_b32_e32 v11, 0xff00ff, v158
	v_lshrrev_b32_e32 v19, 8, v158
	v_and_b32_e32 v12, 0xff00ff, v157
	v_lshrrev_b32_e32 v20, 8, v157
	v_and_b32_e32 v13, 0xff00ff, v156
	v_lshrrev_b32_e32 v21, 8, v156
	v_and_b32_e32 v14, 0xff00ff, v155
	v_lshrrev_b32_e32 v22, 8, v155
	v_and_b32_e32 v15, 0xff00ff, v154
	v_lshrrev_b32_e32 v23, 8, v154
	v_and_b32_e32 v16, 0xff00ff, v16
	v_and_b32_e32 v17, 0xff00ff, v17
	v_and_b32_e32 v18, 0xff00ff, v18
	v_and_b32_e32 v19, 0xff00ff, v19
	v_and_b32_e32 v20, 0xff00ff, v20
	v_and_b32_e32 v21, 0xff00ff, v21
	v_and_b32_e32 v22, 0xff00ff, v22
	v_and_b32_e32 v23, 0xff00ff, v23
	v_add_u32_dpp v8, v8, v8 quad_perm:[1,0,3,2] row_mask:0xf bank_mask:0xf bound_ctrl:1
	v_add_u32_dpp v9, v9, v9 quad_perm:[1,0,3,2] row_mask:0xf bank_mask:0xf bound_ctrl:1
	v_add_u32_dpp v10, v10, v10 quad_perm:[1,0,3,2] row_mask:0xf bank_mask:0xf bound_ctrl:1
	v_add_u32_dpp v11, v11, v11 quad_perm:[1,0,3,2] row_mask:0xf bank_mask:0xf bound_ctrl:1
	v_add_u32_dpp v12, v12, v12 quad_perm:[1,0,3,2] row_mask:0xf bank_mask:0xf bound_ctrl:1
	v_add_u32_dpp v13, v13, v13 quad_perm:[1,0,3,2] row_mask:0xf bank_mask:0xf bound_ctrl:1
	v_add_u32_dpp v14, v14, v14 quad_perm:[1,0,3,2] row_mask:0xf bank_mask:0xf bound_ctrl:1
	v_add_u32_dpp v15, v15, v15 quad_perm:[1,0,3,2] row_mask:0xf bank_mask:0xf bound_ctrl:1
	v_add_u32_dpp v16, v16, v16 quad_perm:[1,0,3,2] row_mask:0xf bank_mask:0xf bound_ctrl:1
	v_add_u32_dpp v17, v17, v17 quad_perm:[1,0,3,2] row_mask:0xf bank_mask:0xf bound_ctrl:1
	v_add_u32_dpp v18, v18, v18 quad_perm:[1,0,3,2] row_mask:0xf bank_mask:0xf bound_ctrl:1
	v_add_u32_dpp v19, v19, v19 quad_perm:[1,0,3,2] row_mask:0xf bank_mask:0xf bound_ctrl:1
	v_add_u32_dpp v20, v20, v20 quad_perm:[1,0,3,2] row_mask:0xf bank_mask:0xf bound_ctrl:1
	v_add_u32_dpp v21, v21, v21 quad_perm:[1,0,3,2] row_mask:0xf bank_mask:0xf bound_ctrl:1
	v_add_u32_dpp v22, v22, v22 quad_perm:[1,0,3,2] row_mask:0xf bank_mask:0xf bound_ctrl:1
	v_add_u32_dpp v23, v23, v23 quad_perm:[1,0,3,2] row_mask:0xf bank_mask:0xf bound_ctrl:1
	v_add_u32_dpp v8, v8, v8 quad_perm:[2,3,0,1] row_mask:0xf bank_mask:0xf bound_ctrl:1
	v_add_u32_dpp v9, v9, v9 quad_perm:[2,3,0,1] row_mask:0xf bank_mask:0xf bound_ctrl:1
	v_add_u32_dpp v10, v10, v10 quad_perm:[2,3,0,1] row_mask:0xf bank_mask:0xf bound_ctrl:1
	v_add_u32_dpp v11, v11, v11 quad_perm:[2,3,0,1] row_mask:0xf bank_mask:0xf bound_ctrl:1
	v_add_u32_dpp v12, v12, v12 quad_perm:[2,3,0,1] row_mask:0xf bank_mask:0xf bound_ctrl:1
	v_add_u32_dpp v13, v13, v13 quad_perm:[2,3,0,1] row_mask:0xf bank_mask:0xf bound_ctrl:1
	v_add_u32_dpp v14, v14, v14 quad_perm:[2,3,0,1] row_mask:0xf bank_mask:0xf bound_ctrl:1
	v_add_u32_dpp v15, v15, v15 quad_perm:[2,3,0,1] row_mask:0xf bank_mask:0xf bound_ctrl:1
	v_add_u32_dpp v16, v16, v16 quad_perm:[2,3,0,1] row_mask:0xf bank_mask:0xf bound_ctrl:1
	v_add_u32_dpp v17, v17, v17 quad_perm:[2,3,0,1] row_mask:0xf bank_mask:0xf bound_ctrl:1
	v_add_u32_dpp v18, v18, v18 quad_perm:[2,3,0,1] row_mask:0xf bank_mask:0xf bound_ctrl:1
	v_add_u32_dpp v19, v19, v19 quad_perm:[2,3,0,1] row_mask:0xf bank_mask:0xf bound_ctrl:1
	v_add_u32_dpp v20, v20, v20 quad_perm:[2,3,0,1] row_mask:0xf bank_mask:0xf bound_ctrl:1
	v_add_u32_dpp v21, v21, v21 quad_perm:[2,3,0,1] row_mask:0xf bank_mask:0xf bound_ctrl:1
	v_add_u32_dpp v22, v22, v22 quad_perm:[2,3,0,1] row_mask:0xf bank_mask:0xf bound_ctrl:1
	v_add_u32_dpp v23, v23, v23 quad_perm:[2,3,0,1] row_mask:0xf bank_mask:0xf bound_ctrl:1
	v_add_u32_dpp v8, v8, v8 row_half_mirror row_mask:0xf bank_mask:0xf bound_ctrl:1
	v_add_u32_dpp v9, v9, v9 row_half_mirror row_mask:0xf bank_mask:0xf bound_ctrl:1
	v_add_u32_dpp v10, v10, v10 row_half_mirror row_mask:0xf bank_mask:0xf bound_ctrl:1
	v_add_u32_dpp v11, v11, v11 row_half_mirror row_mask:0xf bank_mask:0xf bound_ctrl:1
	v_add_u32_dpp v12, v12, v12 row_half_mirror row_mask:0xf bank_mask:0xf bound_ctrl:1
	v_add_u32_dpp v13, v13, v13 row_half_mirror row_mask:0xf bank_mask:0xf bound_ctrl:1
	v_add_u32_dpp v14, v14, v14 row_half_mirror row_mask:0xf bank_mask:0xf bound_ctrl:1
	v_add_u32_dpp v15, v15, v15 row_half_mirror row_mask:0xf bank_mask:0xf bound_ctrl:1
	v_add_u32_dpp v16, v16, v16 row_half_mirror row_mask:0xf bank_mask:0xf bound_ctrl:1
	v_add_u32_dpp v17, v17, v17 row_half_mirror row_mask:0xf bank_mask:0xf bound_ctrl:1
	v_add_u32_dpp v18, v18, v18 row_half_mirror row_mask:0xf bank_mask:0xf bound_ctrl:1
	v_add_u32_dpp v19, v19, v19 row_half_mirror row_mask:0xf bank_mask:0xf bound_ctrl:1
	v_add_u32_dpp v20, v20, v20 row_half_mirror row_mask:0xf bank_mask:0xf bound_ctrl:1
	v_add_u32_dpp v21, v21, v21 row_half_mirror row_mask:0xf bank_mask:0xf bound_ctrl:1
	v_add_u32_dpp v22, v22, v22 row_half_mirror row_mask:0xf bank_mask:0xf bound_ctrl:1
	v_add_u32_dpp v23, v23, v23 row_half_mirror row_mask:0xf bank_mask:0xf bound_ctrl:1
	v_add_u32_dpp v8, v8, v8 row_mirror row_mask:0xf bank_mask:0xf bound_ctrl:1
	v_add_u32_dpp v9, v9, v9 row_mirror row_mask:0xf bank_mask:0xf bound_ctrl:1
	v_add_u32_dpp v10, v10, v10 row_mirror row_mask:0xf bank_mask:0xf bound_ctrl:1
	v_add_u32_dpp v11, v11, v11 row_mirror row_mask:0xf bank_mask:0xf bound_ctrl:1
	v_add_u32_dpp v12, v12, v12 row_mirror row_mask:0xf bank_mask:0xf bound_ctrl:1
	v_add_u32_dpp v13, v13, v13 row_mirror row_mask:0xf bank_mask:0xf bound_ctrl:1
	v_add_u32_dpp v14, v14, v14 row_mirror row_mask:0xf bank_mask:0xf bound_ctrl:1
	v_add_u32_dpp v15, v15, v15 row_mirror row_mask:0xf bank_mask:0xf bound_ctrl:1
	v_add_u32_dpp v16, v16, v16 row_mirror row_mask:0xf bank_mask:0xf bound_ctrl:1
	v_add_u32_dpp v17, v17, v17 row_mirror row_mask:0xf bank_mask:0xf bound_ctrl:1
	v_add_u32_dpp v18, v18, v18 row_mirror row_mask:0xf bank_mask:0xf bound_ctrl:1
	v_add_u32_dpp v19, v19, v19 row_mirror row_mask:0xf bank_mask:0xf bound_ctrl:1
	v_add_u32_dpp v20, v20, v20 row_mirror row_mask:0xf bank_mask:0xf bound_ctrl:1
	v_add_u32_dpp v21, v21, v21 row_mirror row_mask:0xf bank_mask:0xf bound_ctrl:1
	v_add_u32_dpp v22, v22, v22 row_mirror row_mask:0xf bank_mask:0xf bound_ctrl:1
	v_add_u32_dpp v23, v23, v23 row_mirror row_mask:0xf bank_mask:0xf bound_ctrl:1
	v_mov_b32_dpp v24, v8 row_bcast:15 row_mask:0xa bank_mask:0xf bound_ctrl:1
	v_mov_b32_dpp v25, v9 row_bcast:15 row_mask:0xa bank_mask:0xf bound_ctrl:1
	v_mov_b32_dpp v26, v10 row_bcast:15 row_mask:0xa bank_mask:0xf bound_ctrl:1
	v_mov_b32_dpp v27, v11 row_bcast:15 row_mask:0xa bank_mask:0xf bound_ctrl:1
	v_mov_b32_dpp v28, v12 row_bcast:15 row_mask:0xa bank_mask:0xf bound_ctrl:1
	v_mov_b32_dpp v29, v13 row_bcast:15 row_mask:0xa bank_mask:0xf bound_ctrl:1
	v_mov_b32_dpp v30, v14 row_bcast:15 row_mask:0xa bank_mask:0xf bound_ctrl:1
	v_mov_b32_dpp v31, v15 row_bcast:15 row_mask:0xa bank_mask:0xf bound_ctrl:1
	v_mov_b32_dpp v32, v16 row_bcast:15 row_mask:0xa bank_mask:0xf bound_ctrl:1
	v_mov_b32_dpp v33, v17 row_bcast:15 row_mask:0xa bank_mask:0xf bound_ctrl:1
	v_mov_b32_dpp v130, v18 row_bcast:15 row_mask:0xa bank_mask:0xf bound_ctrl:1
	v_mov_b32_dpp v131, v19 row_bcast:15 row_mask:0xa bank_mask:0xf bound_ctrl:1
	v_mov_b32_dpp v132, v20 row_bcast:15 row_mask:0xa bank_mask:0xf bound_ctrl:1
	v_mov_b32_dpp v133, v21 row_bcast:15 row_mask:0xa bank_mask:0xf bound_ctrl:1
	v_mov_b32_dpp v134, v22 row_bcast:15 row_mask:0xa bank_mask:0xf bound_ctrl:1
	v_mov_b32_dpp v135, v23 row_bcast:15 row_mask:0xa bank_mask:0xf bound_ctrl:1
	s_and_saveexec_b64 s[36:37], vcc
	v_add_u32_e32 v8, v8, v24
	v_add_u32_e32 v9, v9, v25
	v_add_u32_e32 v10, v10, v26
	v_add_u32_e32 v11, v11, v27
	v_add_u32_e32 v12, v12, v28
	v_add_u32_e32 v13, v13, v29
	v_add_u32_e32 v14, v14, v30
	v_add_u32_e32 v15, v15, v31
	v_add_u32_e32 v16, v16, v32
	v_add_u32_e32 v17, v17, v33
	v_add_u32_e32 v18, v18, v130
	v_add_u32_e32 v19, v19, v131
	v_add_u32_e32 v20, v20, v132
	v_add_u32_e32 v21, v21, v133
	v_add_u32_e32 v22, v22, v134
	v_add_u32_e32 v23, v23, v135
	v_cvt_f32_u32_sdwa v24, v8 dst_sel:DWORD dst_unused:UNUSED_PAD src0_sel:WORD_0
	v_cvt_f32_u32_sdwa v25, v8 dst_sel:DWORD dst_unused:UNUSED_PAD src0_sel:WORD_1
	v_cvt_f32_u32_sdwa v26, v16 dst_sel:DWORD dst_unused:UNUSED_PAD src0_sel:WORD_0
	v_cvt_f32_u32_sdwa v27, v16 dst_sel:DWORD dst_unused:UNUSED_PAD src0_sel:WORD_1
	v_cvt_f32_u32_sdwa v28, v9 dst_sel:DWORD dst_unused:UNUSED_PAD src0_sel:WORD_0
	v_cvt_f32_u32_sdwa v29, v9 dst_sel:DWORD dst_unused:UNUSED_PAD src0_sel:WORD_1
	v_cvt_f32_u32_sdwa v30, v17 dst_sel:DWORD dst_unused:UNUSED_PAD src0_sel:WORD_0
	v_cvt_f32_u32_sdwa v31, v17 dst_sel:DWORD dst_unused:UNUSED_PAD src0_sel:WORD_1
	v_cvt_f32_u32_sdwa v32, v10 dst_sel:DWORD dst_unused:UNUSED_PAD src0_sel:WORD_0
	v_cvt_f32_u32_sdwa v33, v10 dst_sel:DWORD dst_unused:UNUSED_PAD src0_sel:WORD_1
	v_cvt_f32_u32_sdwa v130, v18 dst_sel:DWORD dst_unused:UNUSED_PAD src0_sel:WORD_0
	v_cvt_f32_u32_sdwa v131, v18 dst_sel:DWORD dst_unused:UNUSED_PAD src0_sel:WORD_1
	v_cvt_f32_u32_sdwa v132, v11 dst_sel:DWORD dst_unused:UNUSED_PAD src0_sel:WORD_0
	v_cvt_f32_u32_sdwa v133, v11 dst_sel:DWORD dst_unused:UNUSED_PAD src0_sel:WORD_1
	v_cvt_f32_u32_sdwa v134, v19 dst_sel:DWORD dst_unused:UNUSED_PAD src0_sel:WORD_0
	v_cvt_f32_u32_sdwa v135, v19 dst_sel:DWORD dst_unused:UNUSED_PAD src0_sel:WORD_1
	v_cvt_f32_u32_sdwa v136, v12 dst_sel:DWORD dst_unused:UNUSED_PAD src0_sel:WORD_0
	v_cvt_f32_u32_sdwa v137, v12 dst_sel:DWORD dst_unused:UNUSED_PAD src0_sel:WORD_1
	v_cvt_f32_u32_sdwa v138, v20 dst_sel:DWORD dst_unused:UNUSED_PAD src0_sel:WORD_0
	v_cvt_f32_u32_sdwa v139, v20 dst_sel:DWORD dst_unused:UNUSED_PAD src0_sel:WORD_1
	v_cvt_f32_u32_sdwa v140, v13 dst_sel:DWORD dst_unused:UNUSED_PAD src0_sel:WORD_0
	v_cvt_f32_u32_sdwa v141, v13 dst_sel:DWORD dst_unused:UNUSED_PAD src0_sel:WORD_1
	v_cvt_f32_u32_sdwa v142, v21 dst_sel:DWORD dst_unused:UNUSED_PAD src0_sel:WORD_0
	v_cvt_f32_u32_sdwa v143, v21 dst_sel:DWORD dst_unused:UNUSED_PAD src0_sel:WORD_1
	v_cvt_f32_u32_sdwa v144, v14 dst_sel:DWORD dst_unused:UNUSED_PAD src0_sel:WORD_0
	v_cvt_f32_u32_sdwa v145, v14 dst_sel:DWORD dst_unused:UNUSED_PAD src0_sel:WORD_1
	v_cvt_f32_u32_sdwa v146, v22 dst_sel:DWORD dst_unused:UNUSED_PAD src0_sel:WORD_0
	v_cvt_f32_u32_sdwa v147, v22 dst_sel:DWORD dst_unused:UNUSED_PAD src0_sel:WORD_1
	v_cvt_f32_u32_sdwa v148, v15 dst_sel:DWORD dst_unused:UNUSED_PAD src0_sel:WORD_0
	v_cvt_f32_u32_sdwa v149, v15 dst_sel:DWORD dst_unused:UNUSED_PAD src0_sel:WORD_1
	v_cvt_f32_u32_sdwa v150, v23 dst_sel:DWORD dst_unused:UNUSED_PAD src0_sel:WORD_0
	v_cvt_f32_u32_sdwa v151, v23 dst_sel:DWORD dst_unused:UNUSED_PAD src0_sel:WORD_1
	ds_write_b32 v152, v24 offset:236
	ds_write_b32 v152, v25 offset:108
	ds_write_b32 v152, v26 offset:172
	ds_write_b32 v152, v27 offset:44
	ds_write_b32 v152, v28 offset:232
	ds_write_b32 v152, v29 offset:104
	ds_write_b32 v152, v30 offset:168
	ds_write_b32 v152, v31 offset:40
	ds_write_b32 v152, v32 offset:228
	ds_write_b32 v152, v33 offset:100
	ds_write_b32 v152, v130 offset:164
	ds_write_b32 v152, v131 offset:36
	ds_write_b32 v152, v132 offset:224
	ds_write_b32 v152, v133 offset:96
	ds_write_b32 v152, v134 offset:160
	ds_write_b32 v152, v135 offset:32
	ds_write_b32 v152, v136 offset:204
	ds_write_b32 v152, v137 offset:76
	ds_write_b32 v152, v138 offset:140
	ds_write_b32 v152, v139 offset:12
	ds_write_b32 v152, v140 offset:200
	ds_write_b32 v152, v141 offset:72
	ds_write_b32 v152, v142 offset:136
	ds_write_b32 v152, v143 offset:8
	ds_write_b32 v152, v144 offset:196
	ds_write_b32 v152, v145 offset:68
	ds_write_b32 v152, v146 offset:132
	ds_write_b32 v152, v147 offset:4
	ds_write_b32 v152, v148 offset:192
	ds_write_b32 v152, v149 offset:64
	ds_write_b32 v152, v150 offset:128
	ds_write_b32 v152, v151
	s_or_b64 exec, exec, s[36:37]
	s_waitcnt vmcnt(6)
	v_mfma_scale_f32_32x32x64_f8f6f4 v[2:17], v[34:41], v[106:113], 0, v201, v201 op_sel_hi:[0,0,0]
	s_waitcnt vmcnt(4)
	v_mfma_scale_f32_32x32x64_f8f6f4 v[2:17], v[42:49], v[122:129], v[2:17], v201, v201 op_sel_hi:[0,0,0]
	s_waitcnt vmcnt(2)
	v_mfma_scale_f32_32x32x64_f8f6f4 v[2:17], v[50:57], v[114:121], v[2:17], v201, v201 op_sel_hi:[0,0,0]
	s_cmp_eq_u32 s52, 0
	s_cselect_b64 s[36:37], -1, 0
	s_and_b64 vcc, exec, s[36:37]
	s_waitcnt lgkmcnt(0)
	s_barrier
	s_cbranch_vccz .LBB1_93
	v_lshlrev_b32_e32 v32, 2, v194
	ds_read2st64_b32 v[18:19], v32 offset0:136 offset1:137
	ds_read2st64_b32 v[20:21], v32 offset0:128 offset1:129
	ds_read2st64_b32 v[22:23], v32 offset0:138 offset1:139
	ds_read2st64_b32 v[24:25], v32 offset0:140 offset1:141
	ds_read2st64_b32 v[26:27], v32 offset0:142 offset1:143
	ds_read2st64_b32 v[28:29], v32 offset0:130 offset1:131
	ds_read2st64_b32 v[30:31], v32 offset0:132 offset1:133
	ds_read2st64_b32 v[32:33], v32 offset0:134 offset1:135
	s_waitcnt lgkmcnt(7)
	v_add_f32_e32 v18, 0, v18
	s_waitcnt lgkmcnt(6)
	v_add_f32_e32 v20, 0, v20
	v_add_f32_e32 v18, v18, v19
	v_add_f32_e32 v19, v20, v21
	s_waitcnt lgkmcnt(2)
	v_add_f32_e32 v19, v19, v28
	v_add_f32_e32 v19, v19, v29
	s_waitcnt lgkmcnt(1)
	v_add_f32_e32 v19, v19, v30
	v_add_f32_e32 v19, v19, v31
	v_add_f32_e32 v18, v18, v22
	s_waitcnt lgkmcnt(0)
	v_add_f32_e32 v19, v19, v32
	v_lshrrev_b32_e32 v22, 1, v0
	v_add_f32_e32 v18, v18, v23
	v_add_f32_e32 v19, v19, v33
	v_lshlrev_b32_e32 v20, 4, v196
	v_and_b32_e32 v21, 3, v0
	v_and_b32_e32 v22, 12, v22
	v_add_f32_e32 v18, v18, v24
	v_or3_b32 v20, v20, v21, v22
	v_rcp_f32_e32 v22, v19
	v_add_f32_e32 v18, v18, v25
	v_add_f32_e32 v18, v18, v26
	v_lshlrev_b32_e32 v21, 5, v0
	v_lshlrev_b32_e32 v20, 2, v20
	s_movk_i32 s34, 0x80
	v_add_f32_e32 v18, v18, v27
	v_and_or_b32 v20, v21, s34, v20
	v_cmp_lt_f32_e32 vcc, 0, v19
	ds_write_b32 v20, v18 offset:37376
	s_nop 0
	v_cndmask_b32_e32 v18, 0, v22, vcc
	ds_write2st64_b32 v20, v19, v18 offset0:144 offset1:145

.LBB1_97:
	v_mfma_scale_f32_32x32x64_f8f6f4 v[18:33], v[66:73], v[106:113], 0, v203, v203 op_sel_hi:[0,0,0]
	v_exp_f32_e64 v2, -v2
	v_exp_f32_e64 v3, -v3
	v_exp_f32_e64 v4, -v4
	v_exp_f32_e64 v5, -v5
	s_waitcnt lgkmcnt(0)
	v_add_co_u32_e64 v212, s[42:43], v212, v212
	v_add_co_u32_e64 v212, s[48:49], v212, v212
	v_add_co_u32_e64 v212, s[50:51], v212, v212
	v_add_co_u32_e64 v212, s[56:57], v212, v212
	v_fma_f32 v230, v162, v2, 1.0
	v_fma_f32 v229, v163, v3, 1.0
	v_fma_f32 v227, v164, v4, 1.0
	v_fma_f32 v225, v165, v5, 1.0
	v_cndmask_b32_e64 v230, 1.0, v230, s[42:43]
	v_cndmask_b32_e64 v229, 1.0, v229, s[48:49]
	v_cndmask_b32_e64 v227, 1.0, v227, s[50:51]
	v_cndmask_b32_e64 v225, 1.0, v225, s[56:57]

	v_mfma_scale_f32_32x32x64_f8f6f4 v[18:33], v[74:81], v[122:129], v[18:33], v203, v203 op_sel_hi:[0,0,0]
	v_exp_f32_e64 v6, -v6
	v_exp_f32_e64 v7, -v7
	v_exp_f32_e64 v8, -v8
	v_exp_f32_e64 v9, -v9
	v_add_co_u32_e64 v212, s[42:43], v212, v212
	v_add_co_u32_e64 v212, s[48:49], v212, v212
	v_add_co_u32_e64 v212, s[50:51], v212, v212
	v_add_co_u32_e64 v212, s[56:57], v212, v212
	v_fma_f32 v224, v166, v6, 1.0
	v_fma_f32 v223, v167, v7, 1.0
	v_fma_f32 v222, v168, v8, 1.0
	v_fma_f32 v219, v169, v9, 1.0
	v_cndmask_b32_e64 v224, 1.0, v224, s[42:43]
	v_cndmask_b32_e64 v223, 1.0, v223, s[48:49]
	v_cndmask_b32_e64 v222, 1.0, v222, s[50:51]
	v_cndmask_b32_e64 v219, 1.0, v219, s[56:57]

	v_mfma_scale_f32_32x32x64_f8f6f4 v[18:33], v[82:89], v[114:121], v[18:33], v203, v203 op_sel_hi:[0,0,0]
	v_exp_f32_e64 v10, -v10
	v_exp_f32_e64 v11, -v11
	v_exp_f32_e64 v12, -v12
	v_exp_f32_e64 v13, -v13
	v_add_co_u32_e64 v212, s[42:43], v212, v212
	v_add_co_u32_e64 v212, s[48:49], v212, v212
	v_add_co_u32_e64 v212, s[50:51], v212, v212
	v_add_co_u32_e64 v212, s[56:57], v212, v212
	v_fma_f32 v213, v170, v10, 1.0
	v_fma_f32 v214, v171, v11, 1.0
	v_fma_f32 v215, v172, v12, 1.0
	v_fma_f32 v216, v173, v13, 1.0
	v_cndmask_b32_e64 v213, 1.0, v213, s[42:43]
	v_cndmask_b32_e64 v214, 1.0, v214, s[48:49]
	v_cndmask_b32_e64 v215, 1.0, v215, s[50:51]
	v_cndmask_b32_e64 v216, 1.0, v216, s[56:57]

	v_mfma_scale_f32_32x32x64_f8f6f4 v[18:33], v[90:97], v[98:105], v[18:33], v203, v203 op_sel_hi:[0,0,0]
	s_and_b32 s34, s38, 0x78
	s_add_i32 s34, s34, s52
	s_lshl_b32 s34, s34, 13
	s_add_i32 s34, s34, s53
	s_or_b32 s42, s34, 0x400
	buffer_load_dwordx4 v[106:109], v195, s[44:47], s34 offen
	buffer_load_dwordx4 v[110:113], v195, s[44:47], s42 offen
	s_or_b32 s42, s34, 0x800
	s_or_b32 s43, s34, 0xc00
	buffer_load_dwordx4 v[122:125], v195, s[44:47], s42 offen
	buffer_load_dwordx4 v[126:129], v195, s[44:47], s43 offen
	s_or_b32 s42, s34, 0x1000
	s_or_b32 s43, s34, 0x1400
	buffer_load_dwordx4 v[114:117], v195, s[44:47], s42 offen
	buffer_load_dwordx4 v[118:121], v195, s[44:47], s43 offen
	s_or_b32 s42, s34, 0x1800
	s_or_b32 s34, s34, 0x1c00
	buffer_load_dwordx4 v[98:101], v195, s[44:47], s42 offen
	buffer_load_dwordx4 v[102:105], v195, s[44:47], s34 offen
	v_exp_f32_e64 v14, -v14
	v_exp_f32_e64 v15, -v15
	v_exp_f32_e64 v16, -v16
	v_exp_f32_e64 v17, -v17
	v_add_co_u32_e64 v212, s[42:43], v212, v212
	v_add_co_u32_e64 v212, s[48:49], v212, v212
	v_add_co_u32_e64 v212, s[50:51], v212, v212
	v_add_co_u32_e64 v212, s[56:57], v212, v212
	v_fma_f32 v210, v174, v14, 1.0
	v_fma_f32 v209, v175, v15, 1.0
	v_fma_f32 v207, v176, v16, 1.0
	v_fma_f32 v206, v177, v17, 1.0
	v_cndmask_b32_e64 v210, 1.0, v210, s[42:43]
	v_cndmask_b32_e64 v209, 1.0, v209, s[48:49]
	v_cndmask_b32_e64 v207, 1.0, v207, s[50:51]
	v_cndmask_b32_e64 v206, 1.0, v206, s[56:57]

	s_cmp_lg_u32 s55, s40
	s_cbranch_scc1 .LBB1_99
	s_nop 15
	s_nop 1
	v_cndmask_b32_e64 v18, v18, v199, s[0:1]
	v_cndmask_b32_e64 v19, v19, v199, s[2:3]
	v_cndmask_b32_e64 v20, v20, v199, s[4:5]
	v_cndmask_b32_e64 v21, v21, v199, s[6:7]
	v_cndmask_b32_e64 v22, v22, v199, s[8:9]
	v_cndmask_b32_e64 v23, v23, v199, s[10:11]
	v_cndmask_b32_e64 v24, v24, v199, s[12:13]
	v_cndmask_b32_e64 v25, v25, v199, s[14:15]
	v_cndmask_b32_e64 v26, v26, v199, s[16:17]
	v_cndmask_b32_e64 v27, v27, v199, s[18:19]
	v_cndmask_b32_e64 v28, v28, v199, s[20:21]
	v_cndmask_b32_e64 v29, v29, v199, s[22:23]
	v_cndmask_b32_e64 v30, v30, v199, s[24:25]
	v_cndmask_b32_e64 v31, v31, v199, s[26:27]
	v_cndmask_b32_e64 v32, v32, v199, s[28:29]
	v_cndmask_b32_e64 v33, v33, v199, s[30:31]
.LBB1_99:
	s_waitcnt vmcnt(14)
	v_mfma_scale_f32_32x32x64_f8f6f4 v[2:17], v[34:41], v[146:153], 0, v203, v203 op_sel_hi:[0,0,0]
	s_nop 7
	v_exp_f32_e64 v18, -v18
	v_exp_f32_e64 v19, -v19
	v_exp_f32_e64 v20, -v20
	v_exp_f32_e64 v21, -v21
	v_add_co_u32_e64 v212, s[42:43], v212, v212
	v_add_co_u32_e64 v212, s[48:49], v212, v212
	v_add_co_u32_e64 v212, s[50:51], v212, v212
	v_add_co_u32_e64 v212, s[56:57], v212, v212
	v_fma_f32 v236, v178, v18, 1.0
	v_fma_f32 v235, v179, v19, 1.0
	v_fma_f32 v234, v180, v20, 1.0
	v_fma_f32 v233, v181, v21, 1.0
	v_cndmask_b32_e64 v236, 1.0, v236, s[42:43]
	v_cndmask_b32_e64 v235, 1.0, v235, s[48:49]
	v_cndmask_b32_e64 v234, 1.0, v234, s[50:51]
	v_cndmask_b32_e64 v233, 1.0, v233, s[56:57]

	v_exp_f32_e64 v22, -v22
	v_exp_f32_e64 v23, -v23
	v_exp_f32_e64 v24, -v24
	v_exp_f32_e64 v25, -v25
	v_add_co_u32_e64 v212, s[42:43], v212, v212
	v_add_co_u32_e64 v212, s[48:49], v212, v212
	v_add_co_u32_e64 v212, s[50:51], v212, v212
	v_add_co_u32_e64 v212, s[56:57], v212, v212
	v_fma_f32 v232, v182, v22, 1.0
	v_fma_f32 v231, v183, v23, 1.0
	v_fma_f32 v228, v184, v24, 1.0
	v_fma_f32 v226, v185, v25, 1.0
	v_cndmask_b32_e64 v232, 1.0, v232, s[42:43]
	v_cndmask_b32_e64 v231, 1.0, v231, s[48:49]
	v_cndmask_b32_e64 v228, 1.0, v228, s[50:51]
	v_cndmask_b32_e64 v226, 1.0, v226, s[56:57]

	v_exp_f32_e64 v26, -v26
	v_exp_f32_e64 v27, -v27
	v_exp_f32_e64 v28, -v28
	v_exp_f32_e64 v29, -v29
	v_add_co_u32_e64 v212, s[42:43], v212, v212
	v_add_co_u32_e64 v212, s[48:49], v212, v212
	v_add_co_u32_e64 v212, s[50:51], v212, v212
	v_add_co_u32_e64 v212, s[56:57], v212, v212
	v_fma_f32 v217, v186, v26, 1.0
	v_fma_f32 v218, v187, v27, 1.0
	v_fma_f32 v220, v188, v28, 1.0
	v_fma_f32 v221, v189, v29, 1.0
	v_cndmask_b32_e64 v217, 1.0, v217, s[42:43]
	v_cndmask_b32_e64 v218, 1.0, v218, s[48:49]
	v_cndmask_b32_e64 v220, 1.0, v220, s[50:51]
	v_cndmask_b32_e64 v221, 1.0, v221, s[56:57]

	s_waitcnt vmcnt(12)
	v_mfma_scale_f32_32x32x64_f8f6f4 v[2:17], v[42:49], v[154:161], v[2:17], v203, v203 op_sel_hi:[0,0,0]
	v_exp_f32_e64 v30, -v30
	v_exp_f32_e64 v31, -v31
	v_exp_f32_e64 v32, -v32
	v_exp_f32_e64 v33, -v33
	v_add_co_u32_e64 v212, s[42:43], v212, v212
	v_add_co_u32_e64 v212, s[48:49], v212, v212
	v_add_co_u32_e64 v212, s[50:51], v212, v212
	v_add_co_u32_e64 v212, s[56:57], v212, v212
	v_fma_f32 v211, v190, v30, 1.0
	v_fma_f32 v208, v191, v31, 1.0
	v_fma_f32 v205, v192, v32, 1.0
	v_fma_f32 v204, v193, v33, 1.0
	v_cndmask_b32_e64 v211, 1.0, v211, s[42:43]
	v_cndmask_b32_e64 v208, 1.0, v208, s[48:49]
	v_cndmask_b32_e64 v205, 1.0, v205, s[50:51]
	v_cndmask_b32_e64 v204, 1.0, v204, s[56:57]

	v_lshl_add_u32 v18, s54, 8, v200
	ds_read_b32 v212, v18
	s_waitcnt vmcnt(10)
	v_mfma_scale_f32_32x32x64_f8f6f4 v[2:17], v[50:57], v[138:145], v[2:17], v203, v203 op_sel_hi:[0,0,0]
	s_waitcnt vmcnt(8)
	v_mfma_scale_f32_32x32x64_f8f6f4 v[2:17], v[58:65], v[130:137], v[2:17], v203, v203 op_sel_hi:[0,0,0]
	s_cmp_lg_u32 s41, s33
	s_cbranch_scc1 .LBB1_101
	v_cndmask_b32_e64 v2, v2, v198, s[0:1]
	v_cndmask_b32_e64 v3, v3, v198, s[2:3]
	v_cndmask_b32_e64 v4, v4, v198, s[4:5]
	v_cndmask_b32_e64 v5, v5, v198, s[6:7]
	v_cndmask_b32_e64 v6, v6, v198, s[8:9]
	v_cndmask_b32_e64 v7, v7, v198, s[10:11]
	v_cndmask_b32_e64 v8, v8, v198, s[12:13]
	v_cndmask_b32_e64 v9, v9, v198, s[14:15]
	v_cndmask_b32_e64 v10, v10, v198, s[16:17]
	v_cndmask_b32_e64 v11, v11, v198, s[18:19]
	v_cndmask_b32_e64 v12, v12, v198, s[20:21]
	v_cndmask_b32_e64 v13, v13, v198, s[22:23]
	v_cndmask_b32_e64 v14, v14, v198, s[24:25]
	v_cndmask_b32_e64 v15, v15, v198, s[26:27]
	v_cndmask_b32_e64 v16, v16, v198, s[28:29]
	v_cndmask_b32_e64 v17, v17, v198, s[30:31]

.LBB1_105:
	s_or_b64 exec, exec, s[2:3]
	s_andn2_b64 vcc, exec, s[36:37]
	s_waitcnt lgkmcnt(0)
	s_barrier
	s_cbranch_vccnz .LBB1_111
	v_lshl_or_b32 v8, v196, 7, v197
	ds_read_b32 v8, v8 offset:36864
	s_waitcnt lgkmcnt(0)
	v_cmp_lt_f32_e32 vcc, 0, v8
	s_and_saveexec_b64 s[2:3], s[0:1]
	s_cbranch_execz .LBB1_110
	v_mov_b32_e32 v8, 0
	ds_read_b128 v[10:13], v8 offset:37632
	ds_read_b128 v[14:17], v8 offset:37648
	v_readlane_b32 s6, v240, 0
	v_readlane_b32 s7, v240, 1
	v_readlane_b32 s8, v240, 6
	s_ashr_i32 s7, s6, 31
	v_readlane_b32 s10, v240, 8
	v_readlane_b32 s11, v240, 9
	v_readlane_b32 s14, v240, 12
	v_readlane_b32 s15, v240, 13
	s_lshl_b64 s[6:7], s[6:7], 2
	s_mov_b64 s[10:11], s[14:15]
	s_waitcnt lgkmcnt(1)
	v_add_f32_e32 v9, 0, v10
	s_add_u32 s6, s10, s6
	s_flbit_i32_b32 s8, 0
	s_mov_b32 s5, 0
	v_add_f32_e32 v9, v9, v11
	s_addc_u32 s7, s11, s7
	s_bcnt1_i32_b64 s4, vcc
	s_min_u32 s8, s8, 32
	v_add_f32_e32 v9, v9, v12
	s_lshl_b64 s[4:5], s[4:5], s8
	v_add_f32_e32 v9, v9, v13
	s_min_u32 s4, s4, 1
	s_waitcnt lgkmcnt(0)
	v_add_f32_e32 v9, v9, v14
	s_or_b32 s4, s5, s4
	v_add_f32_e32 v9, v9, v15
	v_cvt_f32_u32_e32 v10, s4
	v_add_f32_e32 v9, v9, v16
	v_add_f32_e32 v9, v9, v17
	v_mul_f32_e32 v9, 0x3f317218, v9
	s_sub_i32 s4, 32, s8
	s_mov_b64 s[0:1], exec
	global_store_dword v8, v9, s[6:7] sc1
	v_ldexp_f32 v9, v10, s4
	global_store_dword v8, v9, s[6:7] offset:4 sc1
	v_mbcnt_lo_u32_b32 v9, s0, 0
	v_mbcnt_hi_u32_b32 v9, s1, v9
	v_cmp_eq_u32_e32 vcc, 0, v9
	v_readlane_b32 s9, v240, 7
	v_readlane_b32 s12, v240, 10
	v_readlane_b32 s13, v240, 11
	s_and_saveexec_b64 s[4:5], vcc
	s_cbranch_execz .LBB1_109
	s_bcnt1_i32_b64 s0, s[0:1]
	v_readlane_b32 s8, v240, 2
	v_mov_b32_e32 v10, s0
	v_readlane_b32 s9, v240, 3
	v_readlane_b32 s10, v240, 4
	v_readlane_b32 s11, v240, 5
	s_waitcnt vmcnt(0)
	s_nop 0
	global_atomic_add v10, v8, v10, s[8:9] sc0
	s_waitcnt vmcnt(0)
